# conversion tiles per light workgroup 22->24 (gate/up) and 14->15 (down) after the cheaper conversion tails
# baseline (speedup 1.0000x reference)
; __device__ __forceinline__ void conv_slice(const Ctx& c, int lo0, int n0, int lo1, int n1, int lo2, int n2) {
;     const int tot = n0 + n1 + n2, G = c.G;
;     const int mine = (tot - c.bid + G - 1) / G;
;     if (mine <= 0) return;
;     const int tid = c.tid, w = c.wave, lrow = c.lane >> 5, gp = c.lane & 31;
;     const int rr0 = tid >> 3, kq = tid & 7;
; __device__ __forceinline__ void conv_slice_moe(const Ctx& c, int lo, int n, int nwg, int per_light) {
;     const int extra = nwg % c.G, n_light = extra ? c.G - extra : 0;
;     int nb = n_light * per_light; if (nb > n) nb = n;
;     if (n_light > 0 && c.bid >= extra && nb > 0) { Ctx c2 = c; c2.bid = c.bid - extra; c2.G = n_light; conv_slice(c2, lo, nb, 0, 0, 0, 0); }
.LBB0_853:
	s_abs_i32 s30, s96
	v_cvt_f32_u32_e32 v0, s30
	s_sub_i32 s1, 0, s30
	s_abs_i32 s0, s12
	s_ashr_i32 s13, s12, 31
	v_rcp_iflag_f32_e32 v0, v0
	s_ashr_i32 s31, s96, 31
	v_mul_f32_e32 v0, 0x4f7ffffe, v0
	v_cvt_u32_f32_e32 v0, v0
	s_nop 0
	v_readfirstlane_b32 s34, v0
	s_mul_i32 s1, s1, s34
	s_mul_hi_u32 s1, s34, s1
	s_add_i32 s34, s34, s1
	s_mul_hi_u32 s1, s0, s34
	s_mul_i32 s1, s1, s30
	s_sub_i32 s0, s0, s1
	s_sub_i32 s1, s0, s30
	s_cmp_ge_u32 s0, s30
	s_cselect_b32 s0, s1, s0
	s_sub_i32 s1, s0, s30
	s_cmp_ge_u32 s0, s30
	s_cselect_b32 s0, s1, s0
	s_xor_b32 s0, s0, s13
	s_sub_i32 s1, s0, s13
	s_sub_i32 s0, s96, s1
	s_cmp_lg_u32 s1, 0
	s_cselect_b32 s35, s0, 0
	s_mul_i32 s4, s35, 24
	s_min_i32 s33, s4, 0x1000
	s_cmp_lt_i32 s35, 1
	s_cselect_b64 s[4:5], -1, 0
	s_cmp_lt_i32 s2, s1
	s_cselect_b64 s[6:7], -1, 0
	s_or_b64 s[4:5], s[4:5], s[6:7]
	s_and_b64 vcc, exec, s[4:5]
	s_cbranch_vccnz .LBB0_959
	s_abs_i32 s4, s0
	v_cvt_f32_u32_e32 v0, s4
	s_sub_i32 s59, s2, s1
	s_not_b32 s1, s59
	s_sub_i32 s5, 0, s4
	v_rcp_iflag_f32_e32 v0, v0
	s_add_i32 s1, s0, s1
	s_add_i32 s1, s1, s33
	s_xor_b32 s0, s1, s0
	v_mul_f32_e32 v0, 0x4f7ffffe, v0
	v_cvt_u32_f32_e32 v0, v0
	s_abs_i32 s1, s1
	s_ashr_i32 s0, s0, 31
	v_readfirstlane_b32 s6, v0
	s_mul_i32 s5, s5, s6
	s_mul_hi_u32 s5, s6, s5
	s_add_i32 s6, s6, s5
	s_mul_hi_u32 s5, s1, s6
	s_mul_i32 s6, s5, s4
	s_sub_i32 s1, s1, s6
	s_add_i32 s7, s5, 1
	s_sub_i32 s6, s1, s4
	s_cmp_ge_u32 s1, s4
	s_cselect_b32 s5, s7, s5
	s_cselect_b32 s1, s6, s1
	s_add_i32 s6, s5, 1
	s_cmp_ge_u32 s1, s4
	s_cselect_b32 s1, s6, s5
	s_xor_b32 s1, s1, s0
	s_sub_i32 s37, s1, s0
	s_cmp_lt_i32 s37, 1
	s_cbranch_scc1 .LBB0_959
	s_sub_i32 s38, 0, s33
	s_cmp_ge_i32 s59, s33
	s_cselect_b32 s7, s38, 0x4680
	s_add_i32 s7, s7, s59
	s_cmpk_gt_i32 s7, 0x37f
	s_cbranch_scc0 .LBB0_860
	s_cmpk_gt_u32 s7, 0x47f
	s_cbranch_scc0 .LBB0_861
	s_cmpk_gt_u32 s7, 0x67f
	s_cbranch_scc0 .LBB0_862
	s_cmpk_gt_u32 s7, 0x467f
	s_cbranch_scc0 .LBB0_863
	s_add_i32 s0, s7, 0xffffb980
	s_lshr_b32 s0, s0, 7
	s_mov_b32 s1, 0
	s_lshl_b64 s[0:1], s[0:1], 23
	v_readlane_b32 s20, v254, 0
	v_readlane_b32 s21, v254, 1
	s_add_u32 s4, s20, s0
	s_addc_u32 s5, s21, s1
	s_lshl_b32 s0, s7, 7
	s_and_b32 s26, s0, 0x380
	s_lshl_b32 s0, s7, 4
	v_readlane_b32 s22, v254, 2
	v_readlane_b32 s23, v254, 3
	s_and_b32 s6, s0, 0x780
	s_mov_b64 s[0:1], 0
	s_branch .LBB0_864

; __device__ __forceinline__ void conv_slice(const Ctx& c, int lo0, int n0, int lo1, int n1, int lo2, int n2) {
;     const int tot = n0 + n1 + n2, G = c.G;
;     const int mine = (tot - c.bid + G - 1) / G;
;     if (mine <= 0) return;
;     const int tid = c.tid, w = c.wave, lrow = c.lane >> 5, gp = c.lane & 31;
;     const int rr0 = tid >> 3, kq = tid & 7;
; __device__ __forceinline__ void conv_slice_moe(const Ctx& c, int lo, int n, int nwg, int per_light) {
;     const int extra = nwg % c.G, n_light = extra ? c.G - extra : 0;
;     int nb = n_light * per_light; if (nb > n) nb = n;
;     if (n_light > 0 && c.bid >= extra && nb > 0) { Ctx c2 = c; c2.bid = c.bid - extra; c2.G = n_light; conv_slice(c2, lo, nb, 0, 0, 0, 0); }
.LBB0_1217:
	s_abs_i32 s33, s96
	v_cvt_f32_u32_e32 v0, s33
	s_sub_i32 s1, 0, s33
	s_abs_i32 s0, s6
	s_ashr_i32 s7, s6, 31
	v_rcp_iflag_f32_e32 v0, v0
	s_ashr_i32 s41, s96, 31
	v_mul_f32_e32 v0, 0x4f7ffffe, v0
	v_cvt_u32_f32_e32 v0, v0
	s_nop 0
	v_readfirstlane_b32 s43, v0
	s_mul_i32 s1, s1, s43
	s_mul_hi_u32 s1, s43, s1
	s_add_i32 s43, s43, s1
	s_mul_hi_u32 s1, s0, s43
	s_mul_i32 s1, s1, s33
	s_sub_i32 s0, s0, s1
	s_sub_i32 s1, s0, s33
	s_cmp_ge_u32 s0, s33
	s_cselect_b32 s0, s1, s0
	s_sub_i32 s1, s0, s33
	s_cmp_ge_u32 s0, s33
	s_cselect_b32 s0, s1, s0
	s_xor_b32 s0, s0, s7
	s_sub_i32 s1, s0, s7
	s_sub_i32 s0, s96, s1
	s_cmp_lg_u32 s1, 0
	s_cselect_b32 s44, s0, 0
	s_mul_i32 s12, s44, 15
	s_min_i32 s42, s12, 0xd00
	s_cmp_lt_i32 s44, 1
	s_cselect_b64 s[12:13], -1, 0
	s_cmp_lt_i32 s2, s1
	s_cselect_b64 s[14:15], -1, 0
	s_or_b64 s[12:13], s[12:13], s[14:15]
	s_and_b64 vcc, exec, s[12:13]
	s_cbranch_vccnz .LBB0_1322
	s_abs_i32 s12, s0
	v_cvt_f32_u32_e32 v0, s12
	s_sub_i32 s45, s2, s1
	s_not_b32 s1, s45
	s_sub_i32 s13, 0, s12
	v_rcp_iflag_f32_e32 v0, v0
	s_add_i32 s1, s0, s1
	s_add_i32 s1, s1, s42
	s_xor_b32 s0, s1, s0
	v_mul_f32_e32 v0, 0x4f7ffffe, v0
	v_cvt_u32_f32_e32 v0, v0
	s_abs_i32 s1, s1
	s_ashr_i32 s0, s0, 31
	v_readfirstlane_b32 s14, v0
	s_mul_i32 s13, s13, s14
	s_mul_hi_u32 s13, s14, s13
	s_add_i32 s14, s14, s13
	s_mul_hi_u32 s13, s1, s14
	s_mul_i32 s14, s13, s12
	s_sub_i32 s1, s1, s14
	s_add_i32 s15, s13, 1
	s_sub_i32 s14, s1, s12
	s_cmp_ge_u32 s1, s12
	s_cselect_b32 s13, s15, s13
	s_cselect_b32 s1, s14, s1
	s_add_i32 s14, s13, 1
	s_cmp_ge_u32 s1, s12
	s_cselect_b32 s1, s14, s13
	s_xor_b32 s1, s1, s0
	s_sub_i32 s48, s1, s0
	s_cmp_lt_i32 s48, 1
	s_cbranch_scc1 .LBB0_1322
	s_sub_i32 s49, 0, s42
	s_cmp_ge_i32 s45, s42
	s_cselect_b32 s15, s49, 0x2680
	s_add_i32 s15, s15, s45
	s_cmpk_gt_i32 s15, 0x37f
	s_cbranch_scc0 .LBB0_1224
	v_readlane_b32 s52, v254, 47
	s_cmpk_gt_u32 s15, 0x47f
	v_readlane_b32 s53, v254, 48
	v_readlane_b32 s54, v254, 49
	v_readlane_b32 s55, v254, 50
	v_readlane_b32 s56, v254, 51
	v_readlane_b32 s57, v254, 52
	v_readlane_b32 s58, v254, 53
	v_readlane_b32 s59, v254, 54
	v_readlane_b32 s60, v254, 55
	v_readlane_b32 s61, v254, 56
	v_readlane_b32 s62, v254, 57
	v_readlane_b32 s63, v254, 58
	v_readlane_b32 s64, v254, 59
	v_readlane_b32 s65, v254, 60
	v_readlane_b32 s66, v254, 61
	v_readlane_b32 s67, v254, 62
	s_cbranch_scc0 .LBB0_1225
	s_cmpk_gt_u32 s15, 0x67f
	s_cbranch_scc0 .LBB0_1226
	s_cmpk_gt_u32 s15, 0x467f
	s_cbranch_scc0 .LBB0_1227
	s_add_i32 s0, s15, 0xffffb980
	s_lshr_b32 s0, s0, 7
	s_mov_b32 s1, 0
	s_lshl_b64 s[0:1], s[0:1], 23
	v_readlane_b32 s16, v254, 0
	v_readlane_b32 s17, v254, 1
	s_add_u32 s12, s16, s0
	s_addc_u32 s13, s17, s1
	s_lshl_b32 s0, s15, 7
	s_and_b32 s24, s0, 0x380
	s_lshl_b32 s0, s15, 4
	v_readlane_b32 s18, v254, 2
	v_readlane_b32 s19, v254, 3
	s_and_b32 s14, s0, 0x780
	s_mov_b64 s[0:1], 0
	s_branch .LBB0_1228

; __device__ __forceinline__ void conv_slice(const Ctx& c, int lo0, int n0, int lo1, int n1, int lo2, int n2) {
;     const int tot = n0 + n1 + n2, G = c.G;
;     const int mine = (tot - c.bid + G - 1) / G;
;     if (mine <= 0) return;
;     const int tid = c.tid, w = c.wave, lrow = c.lane >> 5, gp = c.lane & 31;
;     const int rr0 = tid >> 3, kq = tid & 7;
; __device__ __forceinline__ void conv_slice_moe(const Ctx& c, int lo, int n, int nwg, int per_light) {
;     const int extra = nwg % c.G, n_light = extra ? c.G - extra : 0;
;     int nb = n_light * per_light; if (nb > n) nb = n;
;     if (n_light > 0 && c.bid >= extra && nb > 0) { Ctx c2 = c; c2.bid = c.bid - extra; c2.G = n_light; conv_slice(c2, lo, nb, 0, 0, 0, 0); }
.LBB0_2182:
	s_abs_i32 s30, s96
	v_cvt_f32_u32_e32 v0, s30
	s_sub_i32 s1, 0, s30
	s_abs_i32 s0, s12
	s_ashr_i32 s13, s12, 31
	v_rcp_iflag_f32_e32 v0, v0
	s_ashr_i32 s31, s96, 31
	v_mul_f32_e32 v0, 0x4f7ffffe, v0
	v_cvt_u32_f32_e32 v0, v0
	s_nop 0
	v_readfirstlane_b32 s34, v0
	s_mul_i32 s1, s1, s34
	s_mul_hi_u32 s1, s34, s1
	s_add_i32 s34, s34, s1
	s_mul_hi_u32 s1, s0, s34
	s_mul_i32 s1, s1, s30
	s_sub_i32 s0, s0, s1
	s_sub_i32 s1, s0, s30
	s_cmp_ge_u32 s0, s30
	s_cselect_b32 s0, s1, s0
	s_sub_i32 s1, s0, s30
	s_cmp_ge_u32 s0, s30
	s_cselect_b32 s0, s1, s0
	s_xor_b32 s0, s0, s13
	s_sub_i32 s1, s0, s13
	s_sub_i32 s0, s96, s1
	s_cmp_lg_u32 s1, 0
	s_cselect_b32 s35, s0, 0
	s_mul_i32 s4, s35, 24
	s_min_i32 s33, s4, 0x1000
	s_cmp_lt_i32 s35, 1
	s_cselect_b64 s[4:5], -1, 0
	s_cmp_lt_i32 s2, s1
	s_cselect_b64 s[6:7], -1, 0
	s_or_b64 s[4:5], s[4:5], s[6:7]
	s_and_b64 vcc, exec, s[4:5]
	s_cbranch_vccnz .LBB0_2287
	s_abs_i32 s4, s0
	v_cvt_f32_u32_e32 v0, s4
	s_sub_i32 s36, s2, s1
	s_not_b32 s1, s36
	s_sub_i32 s5, 0, s4
	v_rcp_iflag_f32_e32 v0, v0
	s_add_i32 s1, s0, s1
	s_add_i32 s1, s1, s33
	s_xor_b32 s0, s1, s0
	v_mul_f32_e32 v0, 0x4f7ffffe, v0
	v_cvt_u32_f32_e32 v0, v0
	s_abs_i32 s1, s1
	s_ashr_i32 s0, s0, 31
	v_readfirstlane_b32 s6, v0
	s_mul_i32 s5, s5, s6
	s_mul_hi_u32 s5, s6, s5
	s_add_i32 s6, s6, s5
	s_mul_hi_u32 s5, s1, s6
	s_mul_i32 s6, s5, s4
	s_sub_i32 s1, s1, s6
	s_add_i32 s7, s5, 1
	s_sub_i32 s6, s1, s4
	s_cmp_ge_u32 s1, s4
	s_cselect_b32 s5, s7, s5
	s_cselect_b32 s1, s6, s1
	s_add_i32 s6, s5, 1
	s_cmp_ge_u32 s1, s4
	s_cselect_b32 s1, s6, s5
	s_xor_b32 s1, s1, s0
	s_sub_i32 s37, s1, s0
	s_cmp_lt_i32 s37, 1
	s_cbranch_scc1 .LBB0_2287
	s_sub_i32 s38, 0, s33
	s_cmp_ge_i32 s36, s33
	s_cselect_b32 s7, s38, 0x5680
	s_add_i32 s7, s7, s36
	s_cmpk_gt_i32 s7, 0x37f
	s_cbranch_scc0 .LBB0_2189
	v_readlane_b32 s56, v254, 47
	s_cmpk_gt_u32 s7, 0x47f
	v_readlane_b32 s57, v254, 48
	v_readlane_b32 s58, v254, 49
	v_readlane_b32 s59, v254, 50
	v_readlane_b32 s60, v254, 51
	v_readlane_b32 s61, v254, 52
	v_readlane_b32 s62, v254, 53
	v_readlane_b32 s63, v254, 54
	v_readlane_b32 s64, v254, 55
	v_readlane_b32 s65, v254, 56
	v_readlane_b32 s66, v254, 57
	v_readlane_b32 s67, v254, 58
	v_readlane_b32 s68, v254, 59
	v_readlane_b32 s69, v254, 60
	v_readlane_b32 s70, v254, 61
	v_readlane_b32 s71, v254, 62
	s_cbranch_scc0 .LBB0_2190
	s_cmpk_gt_u32 s7, 0x67f
	s_cbranch_scc0 .LBB0_2191
	s_cmpk_gt_u32 s7, 0x467f
	s_cbranch_scc0 .LBB0_2192
	s_add_i32 s0, s7, 0xffffb980
	s_lshr_b32 s0, s0, 7
	s_mov_b32 s1, 0
	s_lshl_b64 s[0:1], s[0:1], 23
	v_readlane_b32 s20, v254, 0
	v_readlane_b32 s21, v254, 1
	s_add_u32 s4, s20, s0
	s_addc_u32 s5, s21, s1
	s_lshl_b32 s0, s7, 7
	s_and_b32 s26, s0, 0x380
	s_lshl_b32 s0, s7, 4
	v_readlane_b32 s22, v254, 2
	v_readlane_b32 s23, v254, 3
	s_and_b32 s6, s0, 0x780
	s_mov_b64 s[0:1], 0
	s_branch .LBB0_2193
